# speedup vs baseline: 1.0134x; 1.0050x over previous
_Z8pam_mainPKDv4_jS1_S1_PKfS3_PDF16_Pf:
	s_load_dwordx8 s[4:11], s[0:1], 0x0
	s_load_dwordx4 s[12:15], s[0:1], 0x20
	s_load_dwordx2 s[16:17], s[0:1], 0x30
	v_and_b32_e32 v1, 63, v0
	v_lshrrev_b32_e32 v3, 6, v0
	v_lshlrev_b32_e32 v2, 4, v1
	v_lshlrev_b32_e32 v4, 2, v1
	v_readfirstlane_b32 s18, v3
	v_and_b32_e32 v3, 31, v1
	v_lshlrev_b32_e32 v5, 2, v3
	s_mul_i32 s19, s2, 54
	s_mul_i32 s20, s2, 3
	s_lshr_b32 s20, s20, 4
	s_mul_i32 s21, s20, 0x120
	s_sub_u32 s21, s19, s21
	s_cmp_ge_u32 s20, 24
	s_cselect_b32 s22, 0x120, 0
	s_add_u32 s22, s22, s21
	s_add_u32 s23, s20, 1
	s_cmp_ge_u32 s23, 24
	s_cselect_b32 s24, 0x120, 0
	s_sub_u32 s25, 0x120, s21
	s_cmp_lt_u32 s25, 54
	s_cselect_b32 s26, 1, 0
	s_mul_i32 s25, s25, 43
	s_lshr_b32 s25, s25, 8
	s_cmp_eq_u32 s26, 1
	s_cselect_b32 s25, s25, 100
	s_mov_b32 s29, s2
	s_mov_b32 s46, 0
	s_mov_b32 s47, 30720
	s_mov_b32 s48, 61440
	s_mov_b32 s27, 0
	s_mov_b32 s28, 1
	s_mov_b32 s68, 0
	s_mul_i32 s30, s18, 0xd00
	s_add_u32 s30, s30, 92160
	v_add_u32_e32 v7, s30, v2
	v_mul_u32_u24_e32 v6, 0x68, v3
	v_lshrrev_b32_e32 v130, 2, v1
	v_and_b32_e32 v130, 8, v130
	v_add3_u32 v6, v6, v130, s30
	v_mov_b32_e32 v150, 0xf149f2ca
	s_waitcnt lgkmcnt(0)
	global_load_dwordx4 v[132:135], v2, s[12:13]
	global_load_dwordx4 v[136:139], v2, s[12:13] offset:1024
	global_load_dword v140, v4, s[12:13] offset:2048
	s_mul_i32 s30, s20, 12
	s_add_u32 s30, s30, s18
	s_add_u32 s31, s20, s26
	s_mul_i32 s31, s31, 12
	s_add_u32 s31, s31, s18
	s_lshl_b32 s36, s30, 10
	s_add_u32 s56, s6, s36
	s_addc_u32 s57, s7, 0
	s_lshl_b32 s36, s31, 10
	s_add_u32 s58, s6, s36
	s_addc_u32 s59, s7, 0
	global_load_dwordx4 v[8:11], v2, s[56:57]
	global_load_dwordx4 v[12:15], v2, s[58:59]
	s_lshl_b32 s36, s30, 7
	s_add_u32 s60, s10, s36
	s_addc_u32 s61, s11, 0
	s_lshl_b32 s36, s31, 7
	s_add_u32 s62, s10, s36
	s_addc_u32 s63, s11, 0
	global_load_dword v141, v5, s[60:61]
	global_load_dword v142, v5, s[62:63]
	s_sub_u32 s30, s27, s25
	s_mul_i32 s30, s30, 6
	s_add_u32 s30, s30, s24
	s_mul_i32 s31, s27, 6
	s_add_u32 s31, s31, s22
	s_cmp_lt_u32 s27, s25
	s_cselect_b32 s30, s31, s30
	s_lshl_b32 s33, s18, 10
	s_lshl_b32 s31, s30, 12
	s_add_u32 s31, s31, s33
	s_add_u32 s50, s8, s31
	s_addc_u32 s51, s9, 0
	s_add_u32 s52, s50, 0x3000
	s_addc_u32 s53, s51, 0
	s_add_u32 s34, s46, s33
	s_mov_b32 m0, s34
	s_add_u32 s35, s34, 0x3000
	global_load_lds_dwordx4 v2, s[50:51]
	s_mov_b32 m0, s35
	s_nop 0
	global_load_lds_dwordx4 v2, s[52:53]
	s_cmp_lt_u32 s18, 6
	s_cbranch_scc0 .Lm_nok_p0
	s_lshl_b32 s31, s30, 10
	s_add_u32 s31, s31, s33
	s_add_u32 s54, s4, s31
	s_addc_u32 s55, s5, 0
	s_add_u32 s34, s34, 24576
	s_mov_b32 m0, s34
	s_nop 0
	global_load_lds_dwordx4 v2, s[54:55]
.Lm_nok_p0:
	s_sub_u32 s30, s28, s25
	s_mul_i32 s30, s30, 6
	s_add_u32 s30, s30, s24
	s_mul_i32 s31, s28, 6
	s_add_u32 s31, s31, s22
	s_cmp_lt_u32 s28, s25
	s_cselect_b32 s30, s31, s30
	s_lshl_b32 s33, s18, 10
	s_lshl_b32 s31, s30, 12
	s_add_u32 s31, s31, s33
	s_add_u32 s50, s8, s31
	s_addc_u32 s51, s9, 0
	s_add_u32 s52, s50, 0x3000
	s_addc_u32 s53, s51, 0
	s_add_u32 s34, s47, s33
	s_mov_b32 m0, s34
	s_add_u32 s35, s34, 0x3000
	global_load_lds_dwordx4 v2, s[50:51]
	s_mov_b32 m0, s35
	s_nop 0
	global_load_lds_dwordx4 v2, s[52:53]
	s_cmp_lt_u32 s18, 6
	s_cbranch_scc0 .Lm_nok_p1
	s_lshl_b32 s31, s30, 10
	s_add_u32 s31, s31, s33
	s_add_u32 s54, s4, s31
	s_addc_u32 s55, s5, 0
	s_add_u32 s34, s34, 24576
	s_mov_b32 m0, s34
	s_nop 0
	global_load_lds_dwordx4 v2, s[54:55]
.Lm_nok_p1:
	s_waitcnt vmcnt(4)
	s_nop 0
	v_max3_f32 v132, v132, v133, v134
	v_max3_f32 v136, v136, v137, v138
	v_max3_f32 v132, v132, v135, v139
	v_max3_f32 v132, v132, v136, v140
	s_nop 1
	v_max_f32_dpp v132, v132, v132 quad_perm:[1,0,3,2] row_mask:0xf bank_mask:0xf
	s_nop 1
	v_max_f32_dpp v132, v132, v132 quad_perm:[2,3,0,1] row_mask:0xf bank_mask:0xf
	s_nop 1
	v_max_f32_dpp v132, v132, v132 row_half_mirror row_mask:0xf bank_mask:0xf
	s_nop 1
	v_max_f32_dpp v132, v132, v132 row_mirror row_mask:0xf bank_mask:0xf
	s_nop 1
	v_readlane_b32 s36, v132, 0
	v_readlane_b32 s37, v132, 16
	v_readlane_b32 s38, v132, 32
	v_readlane_b32 s39, v132, 48
	s_nop 2
	v_mov_b32_e32 v133, s36
	v_max_f32_e32 v133, s37, v133
	v_max_f32_e32 v133, s38, v133
	v_max_f32_e32 v133, s39, v133
	s_mov_b32 s37, 0xf800000
	v_mul_f32_e32 v137, 0x4f800000, v133
	v_cmp_gt_f32_e32 vcc, s37, v133
	s_nop 1
	v_cndmask_b32_e32 v133, v133, v137, vcc
	v_sqrt_f32_e32 v137, v133
	s_nop 0
	v_add_u32_e32 v138, -1, v137
	v_add_u32_e32 v139, 1, v137
	v_fma_f32 v143, -v138, v137, v133
	v_fma_f32 v144, -v139, v137, v133
	v_cmp_ge_f32_e64 s[38:39], 0, v143
	s_nop 1
	v_cndmask_b32_e64 v137, v137, v138, s[38:39]
	v_cmp_lt_f32_e64 s[38:39], 0, v144
	s_nop 1
	v_cndmask_b32_e64 v137, v137, v139, s[38:39]
	v_mul_f32_e32 v138, 0x37800000, v137
	v_cndmask_b32_e32 v137, v137, v138, vcc
	v_mov_b32_e32 v138, 0x260
	v_cmp_class_f32_e32 vcc, v133, v138
	s_nop 1
	v_cndmask_b32_e32 v133, v137, v133, vcc
	v_mov_b32_e32 v135, 0x3ca3d70a
	s_mov_b32 s36, 0xffff
	v_mul_f32_e32 v134, v141, v133
	v_mul_f32_e32 v136, v142, v133
	v_fmamk_f32 v134, v134, 0x3f804189, v135
	v_fmamk_f32 v136, v136, 0x3f804189, v135
	v_cvt_f16_f32_e64 v134, -v134
	v_cvt_f16_f32_e64 v136, -v136
	v_cmp_gt_u32_e32 vcc, 32, v1
	v_cvt_f32_f16_e32 v148, v134
	v_cvt_f32_f16_e32 v149, v136
	v_bfi_b32 v134, s36, v134, v11
	v_bfi_b32 v136, s36, v136, v15
	v_cndmask_b32_e32 v11, v11, v134, vcc
	v_cndmask_b32_e32 v15, v15, v136, vcc
	s_waitcnt vmcnt(0)
	s_barrier
	s_mov_b32 s28, 2
	v_add_u32_e32 v128, s46, v2
	v_add_u32_e32 v129, s47, v2
	ds_read_b128 v[88:91], v128 offset:24576
	ds_read_b128 v[92:95], v128 offset:25600
	ds_read_b128 v[96:99], v128 offset:0
	ds_read_b128 v[104:107], v128 offset:2048
	ds_read_b128 v[100:103], v128 offset:1024
	ds_read_b128 v[108:111], v128 offset:3072
	s_sub_u32 s30, s28, s25
	s_mul_i32 s30, s30, 6
	s_add_u32 s30, s30, s24
	s_mul_i32 s31, s28, 6
	s_add_u32 s31, s31, s22
	s_cmp_lt_u32 s28, s25
	s_cselect_b32 s30, s31, s30
	s_lshl_b32 s33, s18, 10
	s_lshl_b32 s31, s30, 12
	s_add_u32 s31, s31, s33
	s_add_u32 s50, s8, s31
	s_addc_u32 s51, s9, 0
	s_add_u32 s52, s50, 0x3000
	s_addc_u32 s53, s51, 0
	s_add_u32 s34, s48, s33
	s_mov_b32 m0, s34
	s_add_u32 s35, s34, 0x3000
	global_load_lds_dwordx4 v2, s[50:51]
	s_mov_b32 m0, s35
	s_nop 0
	global_load_lds_dwordx4 v2, s[52:53]
	s_cmp_lt_u32 s18, 6
	s_cbranch_scc0 .Lm_nok_p2
	s_lshl_b32 s31, s30, 10
	s_add_u32 s31, s31, s33
	s_add_u32 s54, s4, s31
	s_addc_u32 s55, s5, 0
	s_add_u32 s34, s34, 24576
	s_mov_b32 m0, s34
	s_nop 0
	global_load_lds_dwordx4 v2, s[54:55]
